# speedup vs baseline: 1.0055x; 1.0055x over previous
.LBB1_5:
	s_or_b64 exec, exec, s[0:1]
	v_cmp_gt_u32_e32 vcc, 16, v0
	s_waitcnt lgkmcnt(0)
	s_barrier
	s_and_saveexec_b64 s[0:1], vcc
	s_cbranch_execz .LBB1_8
	v_lshlrev_b32_e32 v1, 2, v0
	ds_read_b32 v1, v1
	s_waitcnt lgkmcnt(0)
	s_nop 4
	v_add_f32_dpp v1, v1, v1 quad_perm:[1,0,3,2] row_mask:0xf bank_mask:0xf
	s_nop 1
	v_add_f32_dpp v1, v1, v1 quad_perm:[2,3,0,1] row_mask:0xf bank_mask:0xf
	s_nop 1
	v_add_f32_dpp v1, v1, v1 row_half_mirror row_mask:0xf bank_mask:0xf
	s_nop 1
	v_add_f32_dpp v1, v1, v1 row_mirror row_mask:0xf bank_mask:0xf
	v_cmp_eq_u32_e32 vcc, 0, v0
	s_and_b64 exec, exec, vcc
	s_cbranch_execz .LBB1_8
	v_mul_f32_e32 v0, 0xb8000000, v1
	v_mul_f32_e32 v0, 0x4b000000, v0
	v_rndne_f32_e32 v0, v0
	v_mul_f32_e32 v0, 0x34000000, v0
	v_mov_b32_e32 v16, 0
	global_atomic_add_f32 v16, v0, s[4:5]
